# speedup vs baseline: 1.0084x; 1.0047x over previous
.LBB2_12:
	s_add_i32 s16, s22, 0xffffc000
	s_and_b32 s16, s16, 0xc000
	v_add_u32_e32 v116, s16, v108
	s_add_u32 s16, s12, 0xfffce000
	s_addc_u32 s17, s13, -1
	v_readfirstlane_b32 s26, v116
	v_lshl_add_u64 v[116:117], s[16:17], 0, v[84:85]
	s_mov_b32 s27, m0
	s_mov_b32 m0, s26
	s_nop 0
	global_load_lds_dwordx4 v[116:117], off
	s_mov_b32 m0, s27
	v_lshl_add_u64 v[116:117], s[16:17], 0, v[86:87]
	s_add_i32 s16, s26, 0x400
	s_mov_b32 s17, m0
	s_mov_b32 m0, s16
	s_nop 0
	global_load_lds_dwordx4 v[116:117], off
	s_mov_b32 m0, s17
	s_and_b32 s16, s22, 0xc000
	v_add_u32_e32 v116, s16, v108
	s_nop 0
	v_readfirstlane_b32 s16, v116
	v_lshl_add_u64 v[116:117], s[12:13], 0, v[84:85]
	s_mov_b32 s17, m0
	s_mov_b32 m0, s16
	s_nop 0
	global_load_lds_dwordx4 v[116:117], off
	s_mov_b32 m0, s17
	v_lshl_add_u64 v[116:117], s[12:13], 0, v[86:87]
	s_addk_i32 s16, 0x400
	s_mov_b32 s17, m0
	s_mov_b32 m0, s16
	s_nop 0
	global_load_lds_dwordx4 v[116:117], off
	s_mov_b32 m0, s17
	v_cmp_neq_f32_e32 vcc, s25, v102
	v_add_u32_e32 v114, v114, v98
	v_add_u32_e32 v107, 2, v107
	v_cndmask_b32_e64 v124, v112, -v102, vcc
	v_fmamk_f32 v34, v34, 0x3e38aa3b, v124
	v_fmamk_f32 v50, v50, 0x3e38aa3b, v124
	v_exp_f32_e32 v126, v34
	v_fmamk_f32 v34, v51, 0x3e38aa3b, v124
	v_exp_f32_e32 v125, v50
	v_exp_f32_e32 v82, v34
	v_fmamk_f32 v34, v35, 0x3e38aa3b, v124
	v_exp_f32_e32 v34, v34
	v_add_f32_e32 v35, v126, v125
	v_fmamk_f32 v36, v36, 0x3e38aa3b, v124
	v_exp_f32_e32 v127, v36
	v_pk_add_f32 v[50:51], v[34:35], v[82:83]
	v_fmamk_f32 v35, v52, 0x3e38aa3b, v124
	v_pk_add_f32 v[88:89], v[50:51], v[50:51] op_sel_hi:[0,1]
	v_fmamk_f32 v36, v53, 0x3e38aa3b, v124
	v_exp_f32_e32 v35, v35
	v_exp_f32_e32 v88, v36
	v_fmamk_f32 v36, v37, 0x3e38aa3b, v124
	v_exp_f32_e32 v36, v36
	v_add_f32_e32 v37, v127, v35
	v_fmamk_f32 v38, v38, 0x3e38aa3b, v124
	v_exp_f32_e32 v115, v38
	v_pk_add_f32 v[50:51], v[36:37], v[88:89]
	v_fmamk_f32 v37, v54, 0x3e38aa3b, v124
	v_pk_add_f32 v[90:91], v[50:51], v[50:51] op_sel_hi:[0,1]
	v_fmamk_f32 v38, v55, 0x3e38aa3b, v124
	v_exp_f32_e32 v37, v37
	v_exp_f32_e32 v90, v38
	v_fmamk_f32 v38, v39, 0x3e38aa3b, v124
	v_exp_f32_e32 v50, v38
	v_add_f32_e32 v51, v115, v37
	s_add_u32 s12, s12, 0x64000
	s_addc_u32 s13, s13, 0
	v_pk_add_f32 v[38:39], v[50:51], v[90:91]
	s_add_i32 s22, s22, 0x8000
	v_pk_add_f32 v[54:55], v[38:39], v[38:39] op_sel_hi:[0,1]
	v_fmamk_f32 v38, v56, 0x3e38aa3b, v124
	v_exp_f32_e32 v51, v38
	v_fmamk_f32 v38, v40, 0x3e38aa3b, v124
	v_exp_f32_e32 v91, v38
	v_fmamk_f32 v38, v57, 0x3e38aa3b, v124
	v_exp_f32_e32 v54, v38
	v_fmamk_f32 v38, v41, 0x3e38aa3b, v124
	v_exp_f32_e32 v52, v38
	v_add_f32_e32 v53, v91, v51
	v_cvt_pk_f16_f32 v57, v51, v54
	v_cvt_pk_f16_f32 v56, v37, v90
	v_pk_add_f32 v[38:39], v[52:53], v[54:55]
	v_cvt_pk_f16_f32 v55, v35, v88
	v_pk_add_f32 v[116:117], v[38:39], v[38:39] op_sel_hi:[0,1]
	v_fmamk_f32 v38, v58, 0x3e38aa3b, v124
	v_exp_f32_e32 v53, v38
	v_fmamk_f32 v38, v42, 0x3e38aa3b, v124
	v_exp_f32_e32 v1, v38
	v_fmamk_f32 v38, v59, 0x3e38aa3b, v124
	v_exp_f32_e32 v116, v38
	v_fmamk_f32 v38, v43, 0x3e38aa3b, v124
	v_exp_f32_e32 v38, v38
	v_add_f32_e32 v39, v1, v53
	v_cvt_pk_f16_f32 v54, v125, v82
	v_fmamk_f32 v35, v64, 0x3e38aa3b, v124
	v_pk_add_f32 v[40:41], v[38:39], v[116:117]
	v_fmamk_f32 v39, v60, 0x3e38aa3b, v124
	v_pk_add_f32 v[118:119], v[40:41], v[40:41] op_sel_hi:[0,1]
	v_fmamk_f32 v40, v44, 0x3e38aa3b, v124
	v_exp_f32_e32 v117, v40
	v_fmamk_f32 v40, v61, 0x3e38aa3b, v124
	v_exp_f32_e32 v39, v39
	v_exp_f32_e32 v118, v40
	v_fmamk_f32 v40, v45, 0x3e38aa3b, v124
	v_exp_f32_e32 v40, v40
	v_add_f32_e32 v41, v117, v39
	v_exp_f32_e32 v82, v35
	v_fmamk_f32 v35, v65, 0x3e38aa3b, v124
	v_pk_add_f32 v[42:43], v[40:41], v[118:119]
	v_fmamk_f32 v41, v62, 0x3e38aa3b, v124
	v_pk_add_f32 v[120:121], v[42:43], v[42:43] op_sel_hi:[0,1]
	v_fmamk_f32 v42, v46, 0x3e38aa3b, v124
	v_exp_f32_e32 v119, v42
	v_fmamk_f32 v42, v63, 0x3e38aa3b, v124
	v_exp_f32_e32 v41, v41
	v_exp_f32_e32 v120, v42
	v_fmamk_f32 v42, v47, 0x3e38aa3b, v124
	v_exp_f32_e32 v122, v42
	ds_read_b64_tr_b16 v[42:43], v114 offset:8192
	ds_read_b64_tr_b16 v[44:45], v114 offset:8704
	v_add_f32_e32 v123, v119, v41
	ds_read_b64_tr_b16 v[58:59], v114 offset:9216
	ds_read_b64_tr_b16 v[60:61], v114 offset:9728
	v_pk_add_f32 v[46:47], v[122:123], v[120:121]
	s_waitcnt lgkmcnt(2)
	v_mfma_f32_32x32x16_f16 v[18:33], v[54:57], v[42:45], v[18:33]
	v_add_f32_e64 v88, v46, v46
	v_add_f32_e64 v89, v46, v47
	ds_read_b64_tr_b16 v[42:43], v114 offset:12288
	ds_read_b64_tr_b16 v[44:45], v114 offset:12800
	v_exp_f32_e32 v88, v35
	ds_read_b64_tr_b16 v[62:63], v114 offset:13312
	ds_read_b64_tr_b16 v[64:65], v114 offset:13824
	v_cvt_pk_f16_f32 v51, v127, v36
	v_cmp_le_u32_e32 vcc, s21, v107
	s_or_b64 s[14:15], vcc, s[14:15]
	s_waitcnt lgkmcnt(2)
	v_mfma_f32_32x32x16_f16 v[2:17], v[54:57], v[42:45], v[2:17]
	v_cvt_pk_f16_f32 v45, v82, v88
	v_cvt_pk_f16_f32 v44, v41, v120
	v_cvt_pk_f16_f32 v43, v39, v118
	v_cvt_pk_f16_f32 v42, v53, v116
	v_cvt_pk_f16_f32 v53, v91, v52
	v_cvt_pk_f16_f32 v52, v115, v50
	v_cvt_pk_f16_f32 v50, v126, v34
	v_mfma_f32_32x32x16_f16 v[18:33], v[42:45], v[58:61], v[18:33]
	v_fmamk_f32 v39, v48, 0x3e38aa3b, v124
	v_fmac_f32_e32 v124, 0x3e38aa3b, v49
	v_exp_f32_e32 v39, v39
	v_exp_f32_e32 v54, v124
	v_cvt_pk_f16_f32 v41, v117, v40
	v_cvt_pk_f16_f32 v40, v1, v38
	v_add_f32_e32 v55, v39, v82
	s_waitcnt lgkmcnt(0)
	v_mfma_f32_32x32x16_f16 v[2:17], v[42:45], v[62:65], v[2:17]
	ds_read_b64_tr_b16 v[42:43], v114 offset:10240
	ds_read_b64_tr_b16 v[44:45], v114 offset:10752
	ds_read_b64_tr_b16 v[34:35], v114 offset:11264
	ds_read_b64_tr_b16 v[36:37], v114 offset:11776
	s_waitcnt lgkmcnt(2)
	v_mfma_f32_32x32x16_f16 v[18:33], v[50:53], v[42:45], v[18:33]
	ds_read_b64_tr_b16 v[42:43], v114 offset:14336
	ds_read_b64_tr_b16 v[44:45], v114 offset:14848
	ds_read_b64_tr_b16 v[46:47], v114 offset:15360
	ds_read_b64_tr_b16 v[48:49], v114 offset:15872
	s_waitcnt lgkmcnt(2)
	v_mfma_f32_32x32x16_f16 v[2:17], v[50:53], v[42:45], v[2:17]
	v_cvt_pk_f16_f32 v43, v39, v54
	v_cvt_pk_f16_f32 v42, v119, v122
	s_nop 1
	v_mfma_f32_32x32x16_f16 v[18:33], v[40:43], v[34:37], v[18:33]
	v_add_f32_e64 v34, v54, v88
	v_add_f32_e64 v35, v55, v89
	v_mov_b32_e32 v88, v102
	v_add_f32_e32 v1, v34, v35
	v_add_f32_e32 v113, v113, v1
	s_waitcnt lgkmcnt(0)
	v_mfma_f32_32x32x16_f16 v[2:17], v[40:43], v[46:49], v[2:17]
	s_andn2_b64 exec, exec, s[14:15]
	s_cbranch_execz .LBB2_17
.LBB2_13:
	s_waitcnt vmcnt(0)
	s_barrier
	v_add_u32_e32 v34, s22, v109
	v_add_u32_e32 v34, 0xffff4000, v34
	v_and_b32_e32 v34, 0xc000, v34
	v_add_u32_e32 v114, 0, v34
	v_add_u32_e32 v38, v114, v106
	v_add_u32_e32 v82, v114, v105
	ds_read_b128 v[34:37], v38
	ds_read_b128 v[38:41], v38 offset:4096
	ds_read_b128 v[116:119], v82
	ds_read_b128 v[120:123], v82 offset:4096
	v_add_u32_e32 v82, v114, v104
	s_waitcnt lgkmcnt(2)
	v_mfma_f32_32x32x16_f16 v[50:65], v[34:37], v[78:81], 0
	v_mfma_f32_32x32x16_f16 v[34:49], v[38:41], v[78:81], 0
	s_waitcnt lgkmcnt(1)
	v_mfma_f32_32x32x16_f16 v[50:65], v[116:119], v[74:77], v[50:65]
	s_waitcnt lgkmcnt(0)
	v_mfma_f32_32x32x16_f16 v[34:49], v[120:123], v[74:77], v[34:49]
	ds_read_b128 v[116:119], v82
	ds_read_b128 v[120:123], v82 offset:4096
	v_add_u32_e32 v82, v114, v103
	s_waitcnt lgkmcnt(1)
	v_mfma_f32_32x32x16_f16 v[50:65], v[116:119], v[70:73], v[50:65]
	s_waitcnt lgkmcnt(0)
	v_mfma_f32_32x32x16_f16 v[34:49], v[120:123], v[70:73], v[34:49]
	ds_read_b128 v[116:119], v82
	ds_read_b128 v[120:123], v82 offset:4096
	s_waitcnt lgkmcnt(1)
	v_mfma_f32_32x32x16_f16 v[50:65], v[116:119], v[66:69], v[50:65]
	s_waitcnt lgkmcnt(0)
	v_mfma_f32_32x32x16_f16 v[34:49], v[120:123], v[66:69], v[34:49]
	s_nop 9
	v_max3_f32 v82, v50, v51, v52
	v_max3_f32 v82, v82, v53, v54
	v_max3_f32 v82, v82, v55, v56
	v_max3_f32 v82, v82, v57, v58
	v_max3_f32 v82, v82, v59, v60
	v_max3_f32 v82, v82, v61, v62
	v_max_f32_e32 v91, v65, v65
	v_max3_f32 v89, v34, v35, v36
	v_max3_f32 v89, v89, v37, v38
	v_max3_f32 v89, v89, v39, v40
	v_max3_f32 v89, v89, v41, v42
	v_max3_f32 v89, v89, v43, v44
	v_max3_f32 v89, v89, v45, v46
	v_max_f32_e32 v90, v49, v49
	v_max3_f32 v82, v82, v63, v64
	v_max3_f32 v89, v89, v47, v48
	v_max_f32_e32 v90, v91, v90
	v_max3_f32 v82, v82, v89, v90
	v_mov_b32_e32 v89, v82
	s_nop 1
	v_permlane32_swap_b32_e32 v82, v89
	v_max_f32_e32 v82, v82, v89
	v_fma_f32 v89, v82, s23, -v88
	v_cmp_lt_f32_e32 vcc, s24, v89
	s_cbranch_vccz .LBB2_16
	v_mul_f32_e32 v82, 0x3e38aa3b, v82
	v_max_f32_e32 v82, v82, v82
	v_max_f32_e32 v89, v88, v88
	v_max_f32_e32 v102, v89, v82
	v_sub_f32_e32 v82, v88, v102
	v_exp_f32_e32 v82, v82
	s_and_saveexec_b64 s[16:17], s[4:5]
	s_cbranch_execz .LBB2_11
	v_lshl_add_u32 v88, v95, 2, v100
	ds_write_b32 v88, v82
	s_branch .LBB2_11
